# pq_ra rows-per-wave 14->18: more PEER-table quantisation rows in GEMM1 tail, fewer behind P5 attention (on top of u-side rewrite)
# baseline (speedup 1.0000x reference)
.LBB0_385:
	s_cmp_eq_u32 s43, 0
	s_cbranch_scc1 .LBB0_393
	v_mov_b32_e32 v1, v0
	s_mulk_i32 s45, 0x90
	v_readfirstlane_b32 s2, v1
	s_ashr_i32 s12, s2, 6
	s_min_i32 s5, s45, 0x8000
	s_add_i32 s2, s12, s44
	s_mov_b64 s[6:7], s[0:1]
	s_cmp_ge_i32 s2, s5
	s_cbranch_scc1 .LBB0_393
	s_ashr_i32 s3, s2, 31
	s_waitcnt lgkmcnt(0)
	s_add_i32 s10, s2, 0xffffc000
	s_cmpk_gt_i32 s2, 0x3fff
	s_movk_i32 s18, 0xa8
	s_cselect_b32 s2, s10, s2
	s_cselect_b32 s10, s18, 0xa0
	s_cselect_b32 s3, 0, s3
	s_add_u32 s10, s6, s10
	s_addc_u32 s11, s7, 0
	s_load_dwordx2 s[14:15], s[10:11], 0x0
	s_lshl_b64 s[2:3], s[2:3], 14
	v_and_b32_e32 v130, 63, v1
	v_mov_b32_e32 v133, 0
	v_lshlrev_b32_e32 v132, 4, v130
	s_waitcnt lgkmcnt(0)
	s_add_u32 s2, s14, s2
	s_addc_u32 s3, s15, s3
	s_waitcnt vmcnt(0)
	v_lshl_add_u64 v[2:3], s[2:3], 0, v[132:133]
	s_movk_i32 s19, 0x1000
	v_add_co_u32_e32 v46, vcc, s19, v2
	s_movk_i32 s13, 0x2000
	s_nop 0
	v_addc_co_u32_e32 v47, vcc, 0, v3, vcc
	v_add_co_u32_e32 v4, vcc, s13, v2
	s_load_dwordx2 s[10:11], s[6:7], 0xc0
	global_load_dwordx4 v[122:125], v132, s[2:3] offset:1024 nt
	global_load_dwordx4 v[86:89], v132, s[2:3] offset:2048 nt
	v_addc_co_u32_e32 v5, vcc, 0, v3, vcc
	global_load_dwordx4 v[82:85], v132, s[2:3] offset:3072 nt
	global_load_dwordx4 v[62:65], v[4:5], off offset:-4096 nt
	global_load_dwordx4 v[42:45], v[46:47], off offset:1024 nt
	global_load_dwordx4 v[38:41], v[46:47], off offset:2048 nt
	global_load_dwordx4 v[30:33], v[4:5], off nt
	global_load_dwordx4 v[26:29], v[4:5], off offset:1024 nt
	global_load_dwordx4 v[22:25], v[4:5], off offset:2048 nt
	global_load_dwordx4 v[18:21], v[4:5], off offset:3072 nt
	s_movk_i32 s13, 0x3000
	v_add_co_u32_e32 v48, vcc, s13, v2
	v_mbcnt_lo_u32_b32 v1, -1, 0
	s_nop 0
	v_addc_co_u32_e32 v49, vcc, 0, v3, vcc
	global_load_dwordx4 v[34:37], v[46:47], off offset:3072 nt
	global_load_dwordx4 v[14:17], v[48:49], off nt
	global_load_dwordx4 v[10:13], v[48:49], off offset:1024 nt
	global_load_dwordx4 v[6:9], v[48:49], off offset:2048 nt
	global_load_dwordx4 v[126:129], v132, s[2:3] nt
	global_load_dwordx4 v[2:5], v[48:49], off offset:3072 nt
	v_mbcnt_hi_u32_b32 v46, -1, v1
	v_and_b32_e32 v1, 64, v46
	v_add_u32_e32 v47, 64, v1
	v_xor_b32_e32 v1, 1, v46
	v_cmp_lt_i32_e32 vcc, v1, v47
	v_xor_b32_e32 v48, 2, v46
	s_lshl_b32 s13, s43, 3
	v_cndmask_b32_e32 v1, v46, v1, vcc
	v_cmp_lt_i32_e32 vcc, v48, v47
	s_sub_i32 s21, s12, s13
	s_lshl_b32 s13, s42, 3
	v_cndmask_b32_e32 v48, v46, v48, vcc
	v_lshlrev_b32_e32 v131, 2, v48
	v_xor_b32_e32 v48, 4, v46
	v_cmp_lt_i32_e32 vcc, v48, v47
	s_lshl_b32 s20, s33, 3
	s_add_i32 s12, s12, s13
	v_cndmask_b32_e32 v48, v46, v48, vcc
	v_lshlrev_b32_e32 v134, 2, v48
	v_xor_b32_e32 v48, 8, v46
	v_cmp_lt_i32_e32 vcc, v48, v47
	s_lshl_b32 s13, s43, 4
	s_sub_i32 s22, s12, s13
	v_cndmask_b32_e32 v48, v46, v48, vcc
	v_lshlrev_b32_e32 v135, 2, v48
	v_xor_b32_e32 v48, 16, v46
	v_cmp_lt_i32_e32 vcc, v48, v47
	s_add_i32 s12, s12, s20
	s_sub_i32 s23, s12, s13
	v_cndmask_b32_e32 v48, v46, v48, vcc
	v_lshlrev_b32_e32 v136, 2, v48
	v_xor_b32_e32 v48, 32, v46
	v_cmp_lt_i32_e32 vcc, v48, v47
	v_lshlrev_b32_e32 v1, 2, v1
	v_cmp_eq_u32_e64 s[2:3], 0, v130
	v_cndmask_b32_e32 v46, v46, v48, vcc
	v_lshlrev_b32_e32 v137, 2, v46
	s_ashr_i32 s24, s23, 31
	s_ashr_i32 s25, s4, 31
	s_mov_b32 s26, 0x42fe0000
	s_mov_b32 s27, 0x17c00000
	s_mov_b32 s28, 0xc0c0400
	s_mov_b32 s29, 0x5040100
	s_mov_b32 s30, 0x38d90000
	s_branch .LBB0_389

.LBB0_1000:
	s_cmp_gt_i32 s8, -1
	s_cbranch_scc1 .LBB0_1008
	s_waitcnt lgkmcnt(0)
	s_abs_i32 s2, s58
	v_cvt_f32_u32_e32 v2, s2
	s_sub_i32 s3, 0, s2
	s_ashr_i32 s9, s4, 6
	s_mov_b64 s[4:5], s[0:1]
	v_rcp_iflag_f32_e32 v2, v2
	s_nop 0
	v_mul_f32_e32 v2, 0x4f7ffffe, v2
	v_cvt_u32_f32_e32 v2, v2
	s_nop 0
	v_readfirstlane_b32 s6, v2
	s_mul_i32 s3, s3, s6
	s_mul_hi_u32 s3, s6, s3
	s_add_i32 s6, s6, s3
	s_mul_hi_u32 s3, s6, 0x960
	s_mul_i32 s3, s3, s2
	s_sub_i32 s3, 0x960, s3
	s_sub_i32 s6, s3, s2
	s_cmp_ge_u32 s3, s2
	s_cselect_b32 s3, s6, s3
	s_sub_i32 s6, s3, s2
	s_cmp_ge_u32 s3, s2
	s_cselect_b32 s2, s6, s3
	s_sub_i32 s3, s58, s2
	s_mulk_i32 s3, 0x90
	s_min_i32 s3, s3, 0x8000
	s_cmp_lg_u32 s2, 0
	s_cselect_b32 s10, s3, 0
	s_not_b32 s2, s8
	s_lshl_b32 s2, s2, 3
	s_add_i32 s2, s2, s9
	s_add_i32 s2, s2, s10
	s_cmpk_gt_i32 s2, 0x7fff
	s_cbranch_scc1 .LBB0_1008
	s_lshl_b32 s14, s58, 3
	s_add_i32 s15, s14, 0xffffff00
	s_ashr_i32 s3, s2, 31
	s_add_i32 s6, s2, 0xffffc000
	s_cmpk_gt_i32 s2, 0x3fff
	s_movk_i32 s16, 0xa8
	s_cselect_b32 s2, s6, s2
	s_cselect_b32 s6, s16, 0xa0
	s_cselect_b32 s3, 0, s3
	s_add_u32 s6, s4, s6
	s_addc_u32 s7, s5, 0
	s_load_dwordx2 s[12:13], s[6:7], 0x0
	s_lshl_b64 s[2:3], s[2:3], 14
	v_and_b32_e32 v130, 63, v1
	v_mov_b32_e32 v133, 0
	v_lshlrev_b32_e32 v132, 4, v130
	s_waitcnt lgkmcnt(0)
	s_add_u32 s2, s12, s2
	s_addc_u32 s3, s13, s3
	v_lshl_add_u64 v[2:3], s[2:3], 0, v[132:133]
	s_movk_i32 s17, 0x1000
	v_add_co_u32_e32 v46, vcc, s17, v2
	s_movk_i32 s11, 0x2000
	s_nop 0
	v_addc_co_u32_e32 v47, vcc, 0, v3, vcc
	v_add_co_u32_e32 v4, vcc, s11, v2
	s_load_dwordx2 s[6:7], s[4:5], 0xc0
	global_load_dwordx4 v[122:125], v132, s[2:3] offset:1024 nt
	global_load_dwordx4 v[102:105], v132, s[2:3] offset:2048 nt
	v_addc_co_u32_e32 v5, vcc, 0, v3, vcc
	global_load_dwordx4 v[82:85], v132, s[2:3] offset:3072 nt
	global_load_dwordx4 v[62:65], v[4:5], off offset:-4096 nt
	global_load_dwordx4 v[42:45], v[46:47], off offset:1024 nt
	global_load_dwordx4 v[38:41], v[46:47], off offset:2048 nt
	global_load_dwordx4 v[30:33], v[4:5], off nt
	global_load_dwordx4 v[26:29], v[4:5], off offset:1024 nt
	global_load_dwordx4 v[22:25], v[4:5], off offset:2048 nt
	global_load_dwordx4 v[18:21], v[4:5], off offset:3072 nt
	s_movk_i32 s11, 0x3000
	v_add_co_u32_e32 v48, vcc, s11, v2
	v_mbcnt_lo_u32_b32 v1, -1, 0
	s_nop 0
	v_addc_co_u32_e32 v49, vcc, 0, v3, vcc
	global_load_dwordx4 v[34:37], v[46:47], off offset:3072 nt
	global_load_dwordx4 v[14:17], v[48:49], off nt
	global_load_dwordx4 v[10:13], v[48:49], off offset:1024 nt
	global_load_dwordx4 v[6:9], v[48:49], off offset:2048 nt
	global_load_dwordx4 v[126:129], v132, s[2:3] nt
	global_load_dwordx4 v[2:5], v[48:49], off offset:3072 nt
	v_mbcnt_hi_u32_b32 v46, -1, v1
	v_and_b32_e32 v1, 64, v46
	v_add_u32_e32 v47, 64, v1
	v_xor_b32_e32 v1, 1, v46
	v_cmp_lt_i32_e32 vcc, v1, v47
	v_xor_b32_e32 v48, 2, v46
	s_add_i32 s9, s10, s9
	v_cndmask_b32_e32 v1, v46, v1, vcc
	v_cmp_lt_i32_e32 vcc, v48, v47
	s_lshl_b32 s8, s8, 3
	s_sub_i32 s18, s9, s8
	v_cndmask_b32_e32 v48, v46, v48, vcc
	v_lshlrev_b32_e32 v131, 2, v48
	v_xor_b32_e32 v48, 4, v46
	v_cmp_lt_i32_e32 vcc, v48, v47
	s_add_i32 s9, s9, s14
	s_sub_i32 s8, s9, s8
	v_cndmask_b32_e32 v48, v46, v48, vcc
	v_lshlrev_b32_e32 v134, 2, v48
	v_xor_b32_e32 v48, 8, v46
	v_cmp_lt_i32_e32 vcc, v48, v47
	s_add_i32 s19, s8, 0xfffffef8
	v_lshlrev_b32_e32 v1, 2, v1
	v_cndmask_b32_e32 v48, v46, v48, vcc
	v_lshlrev_b32_e32 v135, 2, v48
	v_xor_b32_e32 v48, 16, v46
	v_cmp_lt_i32_e32 vcc, v48, v47
	v_cmp_eq_u32_e64 s[2:3], 0, v130
	s_ashr_i32 s20, s19, 31
	v_cndmask_b32_e32 v48, v46, v48, vcc
	v_lshlrev_b32_e32 v136, 2, v48
	v_xor_b32_e32 v48, 32, v46
	v_cmp_lt_i32_e32 vcc, v48, v47
	s_ashr_i32 s21, s15, 31
	s_mov_b32 s22, 0x42fe0000
	v_cndmask_b32_e32 v46, v46, v48, vcc
	v_lshlrev_b32_e32 v137, 2, v46
	s_mov_b32 s23, 0x17c00000
	s_mov_b32 s24, 0xc0c0400
	s_mov_b32 s25, 0x5040100
	s_mov_b32 s26, 0x38d90000
	s_branch .LBB0_1004
